# speedup vs baseline: 1.0072x; 1.0038x over previous
.LBB0_742:
	s_or_b64 exec, exec, s[80:81]
	ds_bpermute_b32 v41, v241, v120
	ds_bpermute_b32 v40, v241, v119
	ds_bpermute_b32 v7, v241, v118
	v_mov_b32_e32 v42, v114
	v_mov_b32_e32 v43, v94
	s_waitcnt lgkmcnt(2)
	v_max_f32_e64 v41, |v41|, |v41|
	v_max_f32_e32 v45, 1.0, v41
	ds_bpermute_b32 v41, v241, v121
	s_waitcnt lgkmcnt(2)
	v_max_f32_e64 v40, |v40|, |v40|
	v_max_f32_e32 v40, 1.0, v40
	s_waitcnt lgkmcnt(1)
	v_max_f32_e64 v7, |v7|, |v7|
	v_max_f32_e32 v7, 1.0, v7
	s_waitcnt lgkmcnt(0)
	v_max_f32_e64 v41, |v41|, |v41|
	v_max_f32_e32 v47, 1.0, v41
	v_div_scale_f32 v41, s[80:81], v40, v40, 1.0
	v_rcp_f32_e32 v49, v41
	v_mov_b32_e32 v94, v115
	s_waitcnt lgkmcnt(0)
	s_barrier
	v_fma_f32 v51, -v41, v49, 1.0
	v_fmac_f32_e32 v49, v51, v49
	v_div_scale_f32 v51, vcc, 1.0, v40, 1.0
	v_mul_f32_e32 v52, v51, v49
	v_fma_f32 v53, -v41, v52, v51
	v_fmac_f32_e32 v52, v53, v49
	v_fma_f32 v41, -v41, v52, v51
	v_div_fmas_f32 v41, v41, v49, v52
	v_div_fixup_f32 v53, v41, v40, 1.0
	v_div_scale_f32 v40, s[80:81], v7, v7, 1.0
	v_rcp_f32_e32 v41, v40
	s_nop 0
	v_fma_f32 v49, -v40, v41, 1.0
	v_fmac_f32_e32 v41, v49, v41
	v_div_scale_f32 v49, vcc, 1.0, v7, 1.0
	v_mul_f32_e32 v51, v49, v41
	v_fma_f32 v52, -v40, v51, v49
	v_fmac_f32_e32 v51, v52, v41
	v_fma_f32 v40, -v40, v51, v49
	v_div_fmas_f32 v40, v40, v41, v51
	v_div_fixup_f32 v52, v40, v7, 1.0
	v_div_scale_f32 v7, s[80:81], v47, v47, 1.0
	v_pk_mul_f32 v[122:123], v[74:75], v[52:53]
	v_pk_mul_f32 v[74:75], v[42:43], v[52:53] op_sel_hi:[1,0]
	v_rcp_f32_e32 v42, v7
	v_pk_mul_f32 v[128:129], v[62:63], v[52:53]
	v_pk_mul_f32 v[132:133], v[54:55], v[52:53]
	v_pk_mul_f32 v[40:41], v[128:129], v[128:129]
	v_fma_f32 v43, -v7, v42, 1.0
	v_fmac_f32_e32 v42, v43, v42
	v_div_scale_f32 v43, vcc, 1.0, v47, 1.0
	v_mul_f32_e32 v49, v43, v42
	v_fma_f32 v51, -v7, v49, v43
	v_fmac_f32_e32 v49, v51, v42
	v_fma_f32 v7, -v7, v49, v43
	v_div_fmas_f32 v7, v7, v42, v49
	v_div_fixup_f32 v143, v7, v47, 1.0
	v_div_scale_f32 v7, s[80:81], v45, v45, 1.0
	v_rcp_f32_e32 v42, v7
	v_pk_fma_f32 v[40:41], v[132:133], v[132:133], v[40:41]
	v_pk_mul_f32 v[124:125], v[58:59], v[52:53]
	v_pk_mul_f32 v[120:121], v[70:71], v[52:53]
	v_fma_f32 v43, -v7, v42, 1.0
	v_fmac_f32_e32 v42, v43, v42
	v_div_scale_f32 v43, vcc, 1.0, v45, 1.0
	v_mul_f32_e32 v47, v43, v42
	v_fma_f32 v49, -v7, v47, v43
	v_pk_fma_f32 v[40:41], v[124:125], v[124:125], v[40:41]
	v_fmac_f32_e32 v47, v49, v42
	v_pk_fma_f32 v[40:41], v[122:123], v[122:123], v[40:41]
	v_fma_f32 v7, -v7, v47, v43
	v_pk_fma_f32 v[40:41], v[120:121], v[120:121], v[40:41]
	v_pk_mul_f32 v[118:119], v[66:67], v[52:53]
	v_div_fmas_f32 v7, v7, v42, v47
	v_pk_fma_f32 v[40:41], v[118:119], v[118:119], v[40:41]
	v_pk_mul_f32 v[114:115], v[78:79], v[52:53]
	v_div_fixup_f32 v142, v7, v45, 1.0
	v_pk_fma_f32 v[54:55], v[114:115], v[114:115], v[40:41]
	v_pk_mul_f32 v[40:41], v[90:91], v[52:53]
	v_pk_mul_f32 v[130:131], v[64:65], v[142:143]
	v_pk_fma_f32 v[54:55], v[40:41], v[40:41], v[54:55]
	v_pk_mul_f32 v[86:87], v[86:87], v[52:53]
	v_pk_mul_f32 v[134:135], v[56:57], v[142:143]
	v_pk_mul_f32 v[42:43], v[130:131], v[130:131]
	v_pk_fma_f32 v[54:55], v[86:87], v[86:87], v[54:55]
	v_pk_mul_f32 v[78:79], v[82:83], v[52:53]
	v_pk_fma_f32 v[42:43], v[134:135], v[134:135], v[42:43]
	v_pk_mul_f32 v[126:127], v[60:61], v[142:143]
	v_pk_fma_f32 v[136:137], v[78:79], v[78:79], v[54:55]
	v_mov_b32_e32 v54, v53
	v_mov_b32_e32 v58, v116
	v_mov_b32_e32 v59, v96
	v_mov_b32_e32 v96, v117
	v_pk_fma_f32 v[42:43], v[126:127], v[126:127], v[42:43]
	v_pk_mul_f32 v[116:117], v[76:77], v[142:143]
	v_pk_mul_f32 v[70:71], v[94:95], v[54:55] op_sel_hi:[1,0]
	v_pk_fma_f32 v[42:43], v[116:117], v[116:117], v[42:43]
	v_pk_mul_f32 v[94:95], v[72:73], v[142:143]
	v_pk_mul_f32 v[90:91], v[68:69], v[142:143]
	v_pk_fma_f32 v[42:43], v[94:95], v[94:95], v[42:43]
	v_pk_mul_f32 v[82:83], v[80:81], v[142:143]
	v_pk_fma_f32 v[42:43], v[90:91], v[90:91], v[42:43]
	v_pk_mul_f32 v[80:81], v[88:89], v[142:143]
	v_pk_fma_f32 v[56:57], v[82:83], v[82:83], v[42:43]
	v_pk_mul_f32 v[42:43], v[92:93], v[142:143]
	v_pk_mul_f32 v[76:77], v[84:85], v[142:143]
	v_pk_fma_f32 v[56:57], v[42:43], v[42:43], v[56:57]
	v_pk_mul_f32 v[138:139], v[74:75], v[74:75]
	v_pk_fma_f32 v[56:57], v[80:81], v[80:81], v[56:57]
	v_pk_mul_f32 v[140:141], v[70:71], v[70:71]
	v_pk_fma_f32 v[88:89], v[76:77], v[76:77], v[56:57]
	v_mov_b32_e32 v56, v106
	v_mov_b32_e32 v57, v102
	v_pk_mul_f32 v[62:63], v[56:57], v[52:53] op_sel_hi:[1,0]
	v_mov_b32_e32 v56, v108
	v_mov_b32_e32 v57, v104
	v_pk_mul_f32 v[66:67], v[56:57], v[142:143] op_sel_hi:[1,0]
	v_mov_b32_e32 v56, v110
	v_mov_b32_e32 v57, v98
	v_mov_b32_e32 v84, v143
	v_mov_b32_e32 v102, v107
	v_mov_b32_e32 v104, v109
	v_pk_mul_f32 v[56:57], v[56:57], v[52:53] op_sel_hi:[1,0]
	v_mov_b32_e32 v98, v111
	v_mov_b32_e32 v52, v112
	v_mov_b32_e32 v53, v100
	v_mov_b32_e32 v100, v113
	v_pk_mul_f32 v[72:73], v[58:59], v[142:143] op_sel_hi:[1,0]
	v_pk_mul_f32 v[68:69], v[96:97], v[84:85] op_sel_hi:[1,0]
	v_pk_mul_f32 v[64:65], v[102:103], v[54:55] op_sel_hi:[1,0]
	v_pk_mul_f32 v[60:61], v[104:105], v[84:85] op_sel_hi:[1,0]
	v_pk_mul_f32 v[58:59], v[98:99], v[54:55] op_sel_hi:[1,0]
	v_pk_mul_f32 v[54:55], v[52:53], v[142:143] op_sel_hi:[1,0]
	v_pk_mul_f32 v[52:53], v[100:101], v[84:85] op_sel_hi:[1,0]
	v_mov_b32_e32 v85, v138
	v_mov_b32_e32 v138, v141
	v_pk_mul_f32 v[144:145], v[62:63], v[62:63]
	v_pk_mul_f32 v[102:103], v[64:65], v[64:65]
	v_mov_b32_e32 v84, v140
	v_pk_add_f32 v[112:113], v[138:139], v[136:137] op_sel:[0,1] op_sel_hi:[1,0]
	v_pk_mul_f32 v[108:109], v[56:57], v[56:57]
	v_pk_add_f32 v[84:85], v[84:85], v[112:113]
	v_mov_b32_e32 v112, v103
	v_mov_b32_e32 v113, v145
	v_pk_mul_f32 v[98:99], v[58:59], v[58:59]
	v_pk_add_f32 v[84:85], v[112:113], v[84:85]
	v_mov_b32_e32 v103, v144
	v_pk_add_f32 v[84:85], v[102:103], v[84:85]
	v_mov_b32_e32 v102, v99
	v_mov_b32_e32 v103, v109
	v_pk_add_f32 v[84:85], v[102:103], v[84:85]
	v_mov_b32_e32 v99, v108
	v_pk_add_f32 v[84:85], v[98:99], v[84:85]
	ds_bpermute_b32 v99, v242, v85
	ds_bpermute_b32 v98, v242, v84
	v_pk_mul_f32 v[92:93], v[72:73], v[72:73]
	v_pk_mul_f32 v[96:97], v[68:69], v[68:69]
	v_mov_b32_e32 v103, v92
	v_mov_b32_e32 v92, v97
	s_waitcnt lgkmcnt(0)
	v_pk_add_f32 v[84:85], v[84:85], v[98:99]
	ds_bpermute_b32 v99, v243, v85
	ds_bpermute_b32 v98, v243, v84
	v_pk_mul_f32 v[106:107], v[66:67], v[66:67]
	v_pk_mul_f32 v[104:105], v[60:61], v[60:61]
	v_mov_b32_e32 v102, v96
	v_pk_add_f32 v[88:89], v[92:93], v[88:89] op_sel:[0,1] op_sel_hi:[1,0]
	v_mov_b32_e32 v92, v105
	v_pk_add_f32 v[88:89], v[102:103], v[88:89]
	v_mov_b32_e32 v93, v107
	v_pk_mul_f32 v[110:111], v[54:55], v[54:55]
	v_pk_mul_f32 v[100:101], v[52:53], v[52:53]
	v_pk_add_f32 v[88:89], v[92:93], v[88:89]
	v_mov_b32_e32 v105, v106
	s_waitcnt lgkmcnt(0)
	v_pk_add_f32 v[84:85], v[84:85], v[98:99]
	v_pk_add_f32 v[88:89], v[104:105], v[88:89]
	v_mov_b32_e32 v92, v101
	v_mov_b32_e32 v93, v111
	ds_bpermute_b32 v99, v244, v85
	ds_bpermute_b32 v98, v244, v84
	v_pk_add_f32 v[88:89], v[92:93], v[88:89]
	v_mov_b32_e32 v101, v110
	v_pk_add_f32 v[88:89], v[100:101], v[88:89]
	ds_bpermute_b32 v93, v242, v89
	ds_bpermute_b32 v92, v242, v88
	s_waitcnt lgkmcnt(2)
	v_pk_add_f32 v[84:85], v[84:85], v[98:99]
	ds_bpermute_b32 v99, v245, v85
	ds_bpermute_b32 v98, v245, v84
	s_mov_b32 s80, 0x358637bd
	s_waitcnt lgkmcnt(2)
	v_pk_add_f32 v[88:89], v[88:89], v[92:93]
	ds_bpermute_b32 v93, v243, v89
	ds_bpermute_b32 v92, v243, v88
	s_waitcnt lgkmcnt(2)
	v_pk_add_f32 v[84:85], v[84:85], v[98:99]
	v_mov_b64_e32 v[98:99], s[80:81]
	v_pk_fma_f32 v[84:85], v[84:85], s[8:9], v[98:99] op_sel_hi:[1,0,0]
	s_waitcnt lgkmcnt(0)
	v_pk_add_f32 v[88:89], v[88:89], v[92:93]
	v_mul_f32_e32 v7, 0x4b800000, v85
	v_cmp_gt_f32_e64 s[80:81], s42, v85
	ds_bpermute_b32 v93, v244, v89
	ds_bpermute_b32 v92, v244, v88
	v_cndmask_b32_e64 v7, v85, v7, s[80:81]
	v_rsq_f32_e32 v7, v7
	v_cmp_gt_f32_e32 vcc, s42, v84
	s_waitcnt lgkmcnt(0)
	v_pk_add_f32 v[88:89], v[88:89], v[92:93]
	v_mul_f32_e32 v45, 0x45800000, v7
	v_cndmask_b32_e64 v7, v7, v45, s[80:81]
	v_mul_f32_e32 v45, 0x4b800000, v84
	ds_bpermute_b32 v93, v245, v89
	ds_bpermute_b32 v92, v245, v88
	v_cndmask_b32_e32 v45, v84, v45, vcc
	v_rsq_f32_e32 v45, v45
	v_mul_f32_e32 v40, v40, v7
	s_waitcnt lgkmcnt(0)
	v_pk_add_f32 v[88:89], v[88:89], v[92:93]
	v_mul_f32_e32 v47, 0x45800000, v45
	v_pk_fma_f32 v[88:89], v[88:89], s[8:9], v[98:99] op_sel_hi:[1,0,0]
	v_cndmask_b32_e32 v84, v45, v47, vcc
	v_mul_f32_e32 v45, 0x4b800000, v89
	v_cmp_gt_f32_e64 s[80:81], s42, v89
	v_cmp_gt_f32_e32 vcc, s42, v88
	s_nop 0
	v_cndmask_b32_e64 v45, v89, v45, s[80:81]
	v_rsq_f32_e32 v45, v45
	s_nop 0
	v_mul_f32_e32 v47, 0x45800000, v45
	v_cndmask_b32_e64 v85, v45, v47, s[80:81]
	v_mul_f32_e32 v45, 0x4b800000, v88
	v_cndmask_b32_e32 v45, v88, v45, vcc
	v_rsq_f32_e32 v45, v45
	s_nop 0
	v_mul_f32_e32 v47, 0x45800000, v45
	v_cndmask_b32_e32 v88, v45, v47, vcc
	global_load_dword v45, v[194:195], off
	v_mul_f32_e32 v47, v132, v7
	s_waitcnt vmcnt(0)
	v_mul_f32_e32 v47, v45, v47
	v_bfe_u32 v49, v47, 16, 1
	v_add3_u32 v47, v47, v49, s14
	ds_write_b16_d16_hi v238, v47
	v_mul_f32_e32 v47, v133, v84
	v_mul_f32_e32 v47, v45, v47
	v_bfe_u32 v49, v47, 16, 1
	v_add3_u32 v47, v47, v49, s14
	ds_write_b16_d16_hi v238, v47 offset:272
	v_mul_f32_e32 v47, v134, v85
	v_mul_f32_e32 v47, v45, v47
	v_bfe_u32 v49, v47, 16, 1
	v_add3_u32 v47, v47, v49, s14
	ds_write_b16_d16_hi v238, v47 offset:544
	v_mul_f32_e32 v47, v135, v88
	v_mul_f32_e32 v45, v45, v47
	v_bfe_u32 v47, v45, 16, 1
	v_add3_u32 v45, v45, v47, s14
	ds_write_b16_d16_hi v238, v45 offset:816
	global_load_dword v45, v[194:195], off offset:64
	v_mul_f32_e32 v47, v128, v7
	s_waitcnt vmcnt(0)
	v_mul_f32_e32 v47, v45, v47
	v_bfe_u32 v49, v47, 16, 1
	v_add3_u32 v47, v47, v49, s14
	ds_write_b16_d16_hi v238, v47 offset:32
	v_mul_f32_e32 v47, v129, v84
	v_mul_f32_e32 v47, v45, v47
	v_bfe_u32 v49, v47, 16, 1
	v_add3_u32 v47, v47, v49, s14
	ds_write_b16_d16_hi v238, v47 offset:304
	v_mul_f32_e32 v47, v130, v85
	v_mul_f32_e32 v47, v45, v47
	v_bfe_u32 v49, v47, 16, 1
	v_add3_u32 v47, v47, v49, s14
	ds_write_b16_d16_hi v238, v47 offset:576
	v_mul_f32_e32 v47, v131, v88
	v_mul_f32_e32 v45, v45, v47
	v_bfe_u32 v47, v45, 16, 1
	v_add3_u32 v45, v45, v47, s14
	ds_write_b16_d16_hi v238, v45 offset:848
	global_load_dword v45, v[194:195], off offset:128
	v_mul_f32_e32 v47, v124, v7
	s_waitcnt vmcnt(0)
	v_mul_f32_e32 v47, v45, v47
	v_bfe_u32 v49, v47, 16, 1
	v_add3_u32 v47, v47, v49, s14
	ds_write_b16_d16_hi v238, v47 offset:64
	v_mul_f32_e32 v47, v125, v84
	v_mul_f32_e32 v47, v45, v47
	v_bfe_u32 v49, v47, 16, 1
	v_add3_u32 v47, v47, v49, s14
	ds_write_b16_d16_hi v238, v47 offset:336
	v_mul_f32_e32 v47, v126, v85
	v_mul_f32_e32 v47, v45, v47
	v_bfe_u32 v49, v47, 16, 1
	v_add3_u32 v47, v47, v49, s14
	ds_write_b16_d16_hi v238, v47 offset:608
	v_mul_f32_e32 v47, v127, v88
	v_mul_f32_e32 v45, v45, v47
	v_bfe_u32 v47, v45, 16, 1
	v_add3_u32 v45, v45, v47, s14
	ds_write_b16_d16_hi v238, v45 offset:880
	global_load_dword v45, v[194:195], off offset:192
	v_mul_f32_e32 v47, v122, v7
	s_waitcnt vmcnt(0)
	v_mul_f32_e32 v47, v47, v45
	v_bfe_u32 v49, v47, 16, 1
	v_add3_u32 v47, v47, v49, s14
	ds_write_b16_d16_hi v238, v47 offset:96
	v_mul_f32_e32 v47, v123, v84
	v_mul_f32_e32 v47, v47, v45
	v_bfe_u32 v49, v47, 16, 1
	v_add3_u32 v47, v47, v49, s14
	ds_write_b16_d16_hi v238, v47 offset:368
	v_mul_f32_e32 v47, v116, v85
	v_mul_f32_e32 v47, v45, v47
	v_bfe_u32 v49, v47, 16, 1
	v_add3_u32 v47, v47, v49, s14
	ds_write_b16_d16_hi v238, v47 offset:640
	v_mul_f32_e32 v47, v117, v88
	v_mul_f32_e32 v45, v45, v47
	v_bfe_u32 v47, v45, 16, 1
	v_add3_u32 v45, v45, v47, s14
	ds_write_b16_d16_hi v238, v45 offset:912
	global_load_dword v45, v[194:195], off offset:256
	v_mul_f32_e32 v47, v120, v7
	s_waitcnt vmcnt(0)
	v_mul_f32_e32 v47, v47, v45
	v_bfe_u32 v49, v47, 16, 1
	v_add3_u32 v47, v47, v49, s14
	ds_write_b16_d16_hi v238, v47 offset:128
	v_mul_f32_e32 v47, v121, v84
	v_mul_f32_e32 v47, v47, v45
	v_bfe_u32 v49, v47, 16, 1
	v_add3_u32 v47, v47, v49, s14
	ds_write_b16_d16_hi v238, v47 offset:400
	v_mul_f32_e32 v47, v94, v85
	v_mul_f32_e32 v47, v47, v45
	v_bfe_u32 v49, v47, 16, 1
	v_add3_u32 v47, v47, v49, s14
	ds_write_b16_d16_hi v238, v47 offset:672
	v_mul_f32_e32 v47, v95, v88
	v_mul_f32_e32 v45, v47, v45
	v_bfe_u32 v47, v45, 16, 1
	v_add3_u32 v45, v45, v47, s14
	ds_write_b16_d16_hi v238, v45 offset:944
	global_load_dword v45, v[194:195], off offset:320
	v_mul_f32_e32 v47, v118, v7
	s_waitcnt vmcnt(0)
	v_mul_f32_e32 v47, v47, v45
	v_bfe_u32 v49, v47, 16, 1
	v_add3_u32 v47, v47, v49, s14
	ds_write_b16_d16_hi v238, v47 offset:160
	v_mul_f32_e32 v47, v119, v84
	v_mul_f32_e32 v47, v47, v45
	v_bfe_u32 v49, v47, 16, 1
	v_add3_u32 v47, v47, v49, s14
	ds_write_b16_d16_hi v238, v47 offset:432
	v_mul_f32_e32 v47, v90, v85
	v_mul_f32_e32 v47, v47, v45
	v_bfe_u32 v49, v47, 16, 1
	v_add3_u32 v47, v47, v49, s14
	ds_write_b16_d16_hi v238, v47 offset:704
	v_mul_f32_e32 v47, v91, v88
	v_mul_f32_e32 v45, v47, v45
	v_bfe_u32 v47, v45, 16, 1
	v_add3_u32 v45, v45, v47, s14
	ds_write_b16_d16_hi v238, v45 offset:976
	global_load_dword v45, v[194:195], off offset:384
	v_mul_f32_e32 v47, v114, v7
	s_waitcnt vmcnt(0)
	v_mul_f32_e32 v47, v47, v45
	v_bfe_u32 v49, v47, 16, 1
	v_add3_u32 v47, v47, v49, s14
	ds_write_b16_d16_hi v238, v47 offset:192
	v_mul_f32_e32 v47, v115, v84
	v_mul_f32_e32 v47, v47, v45
	v_bfe_u32 v49, v47, 16, 1
	v_add3_u32 v47, v47, v49, s14
	ds_write_b16_d16_hi v238, v47 offset:464
	v_mul_f32_e32 v47, v82, v85
	v_mul_f32_e32 v47, v47, v45
	v_bfe_u32 v49, v47, 16, 1
	v_add3_u32 v47, v47, v49, s14
	ds_write_b16_d16_hi v238, v47 offset:736
	v_mul_f32_e32 v47, v83, v88
	v_mul_f32_e32 v45, v47, v45
	v_bfe_u32 v47, v45, 16, 1
	v_add3_u32 v45, v45, v47, s14
	ds_write_b16_d16_hi v238, v45 offset:1008
	global_load_dword v45, v[194:195], off offset:448
	s_waitcnt vmcnt(0)
	v_mul_f32_e32 v40, v40, v45
	v_bfe_u32 v47, v40, 16, 1
	v_add3_u32 v40, v40, v47, s14
	ds_write_b16_d16_hi v238, v40 offset:224
	v_mul_f32_e32 v40, v41, v84
	v_mul_f32_e32 v40, v40, v45
	v_bfe_u32 v41, v40, 16, 1
	v_add3_u32 v40, v40, v41, s14
	ds_write_b16_d16_hi v238, v40 offset:496
	v_mul_f32_e32 v40, v42, v85
	v_mul_f32_e32 v40, v40, v45
	v_bfe_u32 v41, v40, 16, 1
	v_add3_u32 v40, v40, v41, s14
	ds_write_b16_d16_hi v238, v40 offset:768
	v_mul_f32_e32 v40, v43, v88
	v_mul_f32_e32 v40, v40, v45
	v_bfe_u32 v41, v40, 16, 1
	v_add3_u32 v40, v40, v41, s14
	ds_write_b16_d16_hi v238, v40 offset:1040
	v_ashrrev_i32_e32 v51, 31, v50
	s_and_saveexec_b64 s[80:81], s[76:77]
	s_cbranch_execz .LBB0_746
	v_lshlrev_b32_e32 v45, 16, v36
	v_mul_f32_e32 v45, 0xbfb8aa3b, v45
	v_exp_f32_e32 v82, v45
	v_lshlrev_b32_e32 v45, 16, v37
	ds_read_b128 v[40:43], v239
	v_mul_f32_e32 v45, 0xbfb8aa3b, v45
	v_exp_f32_e32 v83, v45
	v_and_b32_e32 v36, 0xffff0000, v36
	v_and_b32_e32 v37, 0xffff0000, v37
	s_waitcnt lgkmcnt(0)
	v_lshlrev_b32_e32 v47, 16, v41
	v_pk_add_f32 v[82:83], v[82:83], 1.0 op_sel_hi:[1,0]
	v_lshlrev_b32_e32 v45, 16, v40
	v_rcp_f32_e32 v89, v83
	v_mul_f32_e32 v36, 0xbfb8aa3b, v36
	v_mul_f32_e32 v37, 0xbfb8aa3b, v37
	v_exp_f32_e32 v36, v36
	v_mul_f32_e32 v47, v47, v89
	v_rcp_f32_e32 v83, v82
	v_exp_f32_e32 v37, v37
	v_and_b32_e32 v40, 0xffff0000, v40
	v_and_b32_e32 v41, 0xffff0000, v41
	v_pk_add_f32 v[36:37], v[36:37], 1.0 op_sel_hi:[1,0]
	v_mul_f32_e32 v45, v45, v83
	v_rcp_f32_e32 v82, v36
	s_nop 0
	v_mul_f32_e32 v40, v40, v82
	v_rcp_f32_e32 v49, v37
	s_nop 0
	v_mul_f32_e32 v41, v41, v49
	v_and_b32_e32 v37, 0xffff0000, v38
	v_mul_f32_e32 v37, 0xbfb8aa3b, v37
	v_lshlrev_b32_e32 v36, 16, v38
	v_exp_f32_e32 v38, v37
	v_lshlrev_b32_e32 v37, 16, v39
	v_mul_f32_e32 v36, 0xbfb8aa3b, v36
	v_mul_f32_e32 v37, 0xbfb8aa3b, v37
	v_exp_f32_e32 v36, v36
	v_exp_f32_e32 v37, v37
	v_lshlrev_b32_e32 v82, 16, v43
	v_lshlrev_b32_e32 v49, 16, v42
	v_and_b32_e32 v39, 0xffff0000, v39
	v_pk_add_f32 v[36:37], v[36:37], 1.0 op_sel_hi:[1,0]
	v_mul_f32_e32 v39, 0xbfb8aa3b, v39
	v_rcp_f32_e32 v89, v37
	v_exp_f32_e32 v39, v39
	v_and_b32_e32 v42, 0xffff0000, v42
	v_and_b32_e32 v43, 0xffff0000, v43
	v_mul_f32_e32 v82, v82, v89
	v_rcp_f32_e32 v83, v36
	s_nop 0
	v_mul_f32_e32 v49, v49, v83
	v_pk_add_f32 v[36:37], v[38:39], 1.0 op_sel_hi:[1,0]
	s_nop 0
	v_rcp_f32_e32 v39, v36
	s_nop 0
	v_mul_f32_e32 v36, v42, v39
	v_rcp_f32_e32 v39, v37
	s_nop 0
	v_mul_f32_e32 v37, v43, v39
	v_bfe_u32 v38, v37, 16, 1
	v_bfe_u32 v39, v36, 16, 1
	v_bfe_u32 v42, v41, 16, 1
	v_bfe_u32 v43, v40, 16, 1
	v_add3_u32 v40, v40, v43, s14
	v_add3_u32 v41, v41, v42, s14
	v_add3_u32 v36, v36, v39, s14
	v_add3_u32 v37, v37, v38, s14
	v_bfe_u32 v38, v45, 16, 1
	v_bfe_u32 v39, v47, 16, 1
	v_bfe_u32 v42, v49, 16, 1
	v_bfe_u32 v43, v82, 16, 1
	v_add3_u32 v43, v82, v43, s14
	v_add3_u32 v42, v49, v42, s14
	v_add3_u32 v39, v47, v39, s14
	v_add3_u32 v38, v45, v38, s14
	v_lshrrev_b32_e32 v45, 16, v38
	v_lshrrev_b32_e32 v47, 16, v39
	v_lshrrev_b32_e32 v38, 16, v42
	v_lshrrev_b32_e32 v39, 16, v43
	v_and_or_b32 v39, v37, s17, v39
	v_and_or_b32 v38, v36, s17, v38
	v_and_or_b32 v37, v41, s17, v47
	v_and_or_b32 v36, v40, s17, v45
	v_lshlrev_b64 v[40:41], 11, v[50:51]
	v_lshl_add_u64 v[40:41], v[176:177], 0, v[40:41]
	global_store_dwordx4 v[40:41], v[36:39], off sc1
	s_or_b64 exec, exec, s[80:81]
	v_ashrrev_i32_e32 v49, 31, v48
	s_and_saveexec_b64 s[80:81], s[74:75]
	s_cbranch_execnz .LBB0_747

.LBB0_745:
	v_lshlrev_b32_e32 v36, 16, v28
	v_lshlrev_b32_e32 v37, 16, v29
	ds_read_b128 v[32:35], v239 offset:2176
	v_mul_f32_e32 v36, 0xbfb8aa3b, v36
	v_mul_f32_e32 v37, 0xbfb8aa3b, v37
	v_exp_f32_e32 v36, v36
	v_exp_f32_e32 v37, v37
	s_waitcnt lgkmcnt(0)
	v_lshlrev_b32_e32 v39, 16, v33
	v_lshlrev_b32_e32 v38, 16, v32
	v_and_b32_e32 v28, 0xffff0000, v28
	v_pk_add_f32 v[36:37], v[36:37], 1.0 op_sel_hi:[1,0]
	v_and_b32_e32 v29, 0xffff0000, v29
	v_rcp_f32_e32 v41, v37
	v_mul_f32_e32 v28, 0xbfb8aa3b, v28
	v_mul_f32_e32 v29, 0xbfb8aa3b, v29
	v_exp_f32_e32 v28, v28
	v_mul_f32_e32 v37, v39, v41
	v_rcp_f32_e32 v40, v36
	v_exp_f32_e32 v29, v29
	v_and_b32_e32 v32, 0xffff0000, v32
	v_and_b32_e32 v33, 0xffff0000, v33
	v_pk_add_f32 v[28:29], v[28:29], 1.0 op_sel_hi:[1,0]
	v_mul_f32_e32 v36, v38, v40
	v_rcp_f32_e32 v39, v28
	s_nop 0
	v_mul_f32_e32 v32, v32, v39
	v_rcp_f32_e32 v38, v29
	s_nop 0
	v_mul_f32_e32 v33, v33, v38
	v_and_b32_e32 v29, 0xffff0000, v30
	v_mul_f32_e32 v29, 0xbfb8aa3b, v29
	v_lshlrev_b32_e32 v28, 16, v30
	v_exp_f32_e32 v30, v29
	v_lshlrev_b32_e32 v29, 16, v31
	v_mul_f32_e32 v28, 0xbfb8aa3b, v28
	v_mul_f32_e32 v29, 0xbfb8aa3b, v29
	v_exp_f32_e32 v28, v28
	v_exp_f32_e32 v29, v29
	v_lshlrev_b32_e32 v39, 16, v35
	v_lshlrev_b32_e32 v38, 16, v34
	v_and_b32_e32 v31, 0xffff0000, v31
	v_pk_add_f32 v[28:29], v[28:29], 1.0 op_sel_hi:[1,0]
	v_mul_f32_e32 v31, 0xbfb8aa3b, v31
	v_rcp_f32_e32 v41, v29
	v_exp_f32_e32 v31, v31
	v_and_b32_e32 v34, 0xffff0000, v34
	v_and_b32_e32 v35, 0xffff0000, v35
	v_mul_f32_e32 v39, v39, v41
	v_rcp_f32_e32 v40, v28
	s_nop 0
	v_mul_f32_e32 v38, v38, v40
	v_pk_add_f32 v[28:29], v[30:31], 1.0 op_sel_hi:[1,0]
	s_nop 0
	v_rcp_f32_e32 v31, v28
	s_nop 0
	v_mul_f32_e32 v28, v34, v31
	v_rcp_f32_e32 v31, v29
	s_nop 0
	v_mul_f32_e32 v29, v35, v31
	v_bfe_u32 v30, v29, 16, 1
	v_bfe_u32 v31, v28, 16, 1
	v_bfe_u32 v34, v33, 16, 1
	v_bfe_u32 v35, v32, 16, 1
	v_add3_u32 v32, v32, v35, s14
	v_add3_u32 v33, v33, v34, s14
	v_add3_u32 v28, v28, v31, s14
	v_add3_u32 v29, v29, v30, s14
	v_bfe_u32 v30, v36, 16, 1
	v_bfe_u32 v31, v37, 16, 1
	v_bfe_u32 v34, v38, 16, 1
	v_bfe_u32 v35, v39, 16, 1
	v_add3_u32 v35, v39, v35, s14
	v_add3_u32 v34, v38, v34, s14
	v_add3_u32 v31, v37, v31, s14
	v_add3_u32 v30, v36, v30, s14
	v_lshrrev_b32_e32 v36, 16, v30
	v_lshrrev_b32_e32 v37, 16, v31
	v_lshrrev_b32_e32 v30, 16, v34
	v_lshrrev_b32_e32 v31, 16, v35
	v_and_or_b32 v31, v29, s17, v31
	v_and_or_b32 v30, v28, s17, v30
	v_and_or_b32 v29, v33, s17, v37
	v_and_or_b32 v28, v32, s17, v36
	v_lshlrev_b64 v[32:33], 11, v[46:47]
	v_lshl_add_u64 v[32:33], v[176:177], 0, v[32:33]
	global_store_dwordx4 v[32:33], v[28:31], off sc1
	s_or_b64 exec, exec, s[80:81]
	v_ashrrev_i32_e32 v45, 31, v44
	s_and_saveexec_b64 s[80:81], s[70:71]
	s_cbranch_execnz .LBB0_749
	s_branch .LBB0_750

.LBB0_747:
	v_lshlrev_b32_e32 v40, 16, v32
	v_lshlrev_b32_e32 v41, 16, v33
	ds_read_b128 v[36:39], v239 offset:1088
	v_mul_f32_e32 v40, 0xbfb8aa3b, v40
	v_mul_f32_e32 v41, 0xbfb8aa3b, v41
	v_exp_f32_e32 v40, v40
	v_exp_f32_e32 v41, v41
	s_waitcnt lgkmcnt(0)
	v_lshlrev_b32_e32 v43, 16, v37
	v_lshlrev_b32_e32 v42, 16, v36
	v_and_b32_e32 v32, 0xffff0000, v32
	v_pk_add_f32 v[40:41], v[40:41], 1.0 op_sel_hi:[1,0]
	v_and_b32_e32 v33, 0xffff0000, v33
	v_rcp_f32_e32 v47, v41
	v_mul_f32_e32 v32, 0xbfb8aa3b, v32
	v_mul_f32_e32 v33, 0xbfb8aa3b, v33
	v_exp_f32_e32 v32, v32
	v_mul_f32_e32 v41, v43, v47
	v_rcp_f32_e32 v45, v40
	v_exp_f32_e32 v33, v33
	v_and_b32_e32 v36, 0xffff0000, v36
	v_and_b32_e32 v37, 0xffff0000, v37
	v_pk_add_f32 v[32:33], v[32:33], 1.0 op_sel_hi:[1,0]
	v_mul_f32_e32 v40, v42, v45
	v_rcp_f32_e32 v43, v32
	s_nop 0
	v_mul_f32_e32 v36, v36, v43
	v_rcp_f32_e32 v42, v33
	s_nop 0
	v_mul_f32_e32 v37, v37, v42
	v_and_b32_e32 v33, 0xffff0000, v34
	v_mul_f32_e32 v33, 0xbfb8aa3b, v33
	v_lshlrev_b32_e32 v32, 16, v34
	v_exp_f32_e32 v34, v33
	v_lshlrev_b32_e32 v33, 16, v35
	v_mul_f32_e32 v32, 0xbfb8aa3b, v32
	v_mul_f32_e32 v33, 0xbfb8aa3b, v33
	v_exp_f32_e32 v32, v32
	v_exp_f32_e32 v33, v33
	v_lshlrev_b32_e32 v43, 16, v39
	v_lshlrev_b32_e32 v42, 16, v38
	v_and_b32_e32 v35, 0xffff0000, v35
	v_pk_add_f32 v[32:33], v[32:33], 1.0 op_sel_hi:[1,0]
	v_mul_f32_e32 v35, 0xbfb8aa3b, v35
	v_rcp_f32_e32 v47, v33
	v_exp_f32_e32 v35, v35
	v_and_b32_e32 v38, 0xffff0000, v38
	v_and_b32_e32 v39, 0xffff0000, v39
	v_mul_f32_e32 v43, v43, v47
	v_rcp_f32_e32 v45, v32
	s_nop 0
	v_mul_f32_e32 v42, v42, v45
	v_pk_add_f32 v[32:33], v[34:35], 1.0 op_sel_hi:[1,0]
	s_nop 0
	v_rcp_f32_e32 v35, v32
	s_nop 0
	v_mul_f32_e32 v32, v38, v35
	v_rcp_f32_e32 v35, v33
	s_nop 0
	v_mul_f32_e32 v33, v39, v35
	v_bfe_u32 v34, v33, 16, 1
	v_bfe_u32 v35, v32, 16, 1
	v_bfe_u32 v38, v37, 16, 1
	v_bfe_u32 v39, v36, 16, 1
	v_add3_u32 v36, v36, v39, s14
	v_add3_u32 v37, v37, v38, s14
	v_add3_u32 v32, v32, v35, s14
	v_add3_u32 v33, v33, v34, s14
	v_bfe_u32 v34, v40, 16, 1
	v_bfe_u32 v35, v41, 16, 1
	v_bfe_u32 v38, v42, 16, 1
	v_bfe_u32 v39, v43, 16, 1
	v_add3_u32 v39, v43, v39, s14
	v_add3_u32 v38, v42, v38, s14
	v_add3_u32 v35, v41, v35, s14
	v_add3_u32 v34, v40, v34, s14
	v_lshrrev_b32_e32 v40, 16, v34
	v_lshrrev_b32_e32 v41, 16, v35
	v_lshrrev_b32_e32 v34, 16, v38
	v_lshrrev_b32_e32 v35, 16, v39
	v_and_or_b32 v35, v33, s17, v35
	v_and_or_b32 v34, v32, s17, v34
	v_and_or_b32 v33, v37, s17, v41
	v_and_or_b32 v32, v36, s17, v40
	v_lshlrev_b64 v[36:37], 11, v[48:49]
	v_lshl_add_u64 v[36:37], v[176:177], 0, v[36:37]
	global_store_dwordx4 v[36:37], v[32:35], off sc1
	s_or_b64 exec, exec, s[80:81]
	v_ashrrev_i32_e32 v47, 31, v46
	s_and_saveexec_b64 s[80:81], s[72:73]
	s_cbranch_execnz .LBB0_745

.LBB0_749:
	v_lshlrev_b32_e32 v32, 16, v24
	v_lshlrev_b32_e32 v33, 16, v25
	ds_read_b128 v[28:31], v239 offset:3264
	v_mul_f32_e32 v32, 0xbfb8aa3b, v32
	v_mul_f32_e32 v33, 0xbfb8aa3b, v33
	v_exp_f32_e32 v32, v32
	v_exp_f32_e32 v33, v33
	s_waitcnt lgkmcnt(0)
	v_lshlrev_b32_e32 v35, 16, v29
	v_lshlrev_b32_e32 v34, 16, v28
	v_and_b32_e32 v24, 0xffff0000, v24
	v_pk_add_f32 v[32:33], v[32:33], 1.0 op_sel_hi:[1,0]
	v_and_b32_e32 v25, 0xffff0000, v25
	v_rcp_f32_e32 v37, v33
	v_mul_f32_e32 v24, 0xbfb8aa3b, v24
	v_mul_f32_e32 v25, 0xbfb8aa3b, v25
	v_exp_f32_e32 v24, v24
	v_mul_f32_e32 v33, v35, v37
	v_rcp_f32_e32 v36, v32
	v_exp_f32_e32 v25, v25
	v_and_b32_e32 v28, 0xffff0000, v28
	v_and_b32_e32 v29, 0xffff0000, v29
	v_pk_add_f32 v[24:25], v[24:25], 1.0 op_sel_hi:[1,0]
	v_mul_f32_e32 v32, v34, v36
	v_rcp_f32_e32 v35, v24
	s_nop 0
	v_mul_f32_e32 v28, v28, v35
	v_rcp_f32_e32 v34, v25
	s_nop 0
	v_mul_f32_e32 v29, v29, v34
	v_and_b32_e32 v25, 0xffff0000, v26
	v_mul_f32_e32 v25, 0xbfb8aa3b, v25
	v_lshlrev_b32_e32 v24, 16, v26
	v_exp_f32_e32 v26, v25
	v_lshlrev_b32_e32 v25, 16, v27
	v_mul_f32_e32 v24, 0xbfb8aa3b, v24
	v_mul_f32_e32 v25, 0xbfb8aa3b, v25
	v_exp_f32_e32 v24, v24
	v_exp_f32_e32 v25, v25
	v_lshlrev_b32_e32 v35, 16, v31
	v_lshlrev_b32_e32 v34, 16, v30
	v_and_b32_e32 v27, 0xffff0000, v27
	v_pk_add_f32 v[24:25], v[24:25], 1.0 op_sel_hi:[1,0]
	v_mul_f32_e32 v27, 0xbfb8aa3b, v27
	v_rcp_f32_e32 v37, v25
	v_exp_f32_e32 v27, v27
	v_and_b32_e32 v30, 0xffff0000, v30
	v_and_b32_e32 v31, 0xffff0000, v31
	v_mul_f32_e32 v35, v35, v37
	v_rcp_f32_e32 v36, v24
	s_nop 0
	v_mul_f32_e32 v34, v34, v36
	v_pk_add_f32 v[24:25], v[26:27], 1.0 op_sel_hi:[1,0]
	s_nop 0
	v_rcp_f32_e32 v27, v24
	s_nop 0
	v_mul_f32_e32 v24, v30, v27
	v_rcp_f32_e32 v27, v25
	s_nop 0
	v_mul_f32_e32 v25, v31, v27
	v_bfe_u32 v26, v25, 16, 1
	v_bfe_u32 v27, v24, 16, 1
	v_bfe_u32 v30, v29, 16, 1
	v_bfe_u32 v31, v28, 16, 1
	v_add3_u32 v28, v28, v31, s14
	v_add3_u32 v29, v29, v30, s14
	v_add3_u32 v24, v24, v27, s14
	v_add3_u32 v25, v25, v26, s14
	v_bfe_u32 v26, v32, 16, 1
	v_bfe_u32 v27, v33, 16, 1
	v_bfe_u32 v30, v34, 16, 1
	v_bfe_u32 v31, v35, 16, 1
	v_add3_u32 v31, v35, v31, s14
	v_add3_u32 v30, v34, v30, s14
	v_add3_u32 v27, v33, v27, s14
	v_add3_u32 v26, v32, v26, s14
	v_lshrrev_b32_e32 v32, 16, v26
	v_lshrrev_b32_e32 v33, 16, v27
	v_lshrrev_b32_e32 v26, 16, v30
	v_lshrrev_b32_e32 v27, 16, v31
	v_and_or_b32 v27, v25, s17, v27
	v_and_or_b32 v26, v24, s17, v26
	v_and_or_b32 v25, v29, s17, v33
	v_and_or_b32 v24, v28, s17, v32
	v_lshlrev_b64 v[28:29], 11, v[44:45]
	v_lshl_add_u64 v[28:29], v[176:177], 0, v[28:29]
	global_store_dwordx4 v[28:29], v[24:27], off sc1
.LBB0_750:
	s_or_b64 exec, exec, s[80:81]
	global_load_dword v24, v[194:195], off offset:512
	v_mul_f32_e32 v25, v86, v7
	s_waitcnt vmcnt(0)
	v_mul_f32_e32 v25, v25, v24
	v_bfe_u32 v26, v25, 16, 1
	v_add3_u32 v25, v25, v26, s14
	ds_write_b16_d16_hi v238, v25
	v_mul_f32_e32 v25, v87, v84
	v_mul_f32_e32 v25, v25, v24
	v_bfe_u32 v26, v25, 16, 1
	v_add3_u32 v25, v25, v26, s14
	ds_write_b16_d16_hi v238, v25 offset:272
	v_mul_f32_e32 v25, v80, v85
	v_mul_f32_e32 v25, v25, v24
	v_bfe_u32 v26, v25, 16, 1
	v_add3_u32 v25, v25, v26, s14
	ds_write_b16_d16_hi v238, v25 offset:544
	v_mul_f32_e32 v25, v81, v88
	v_mul_f32_e32 v24, v25, v24
	v_bfe_u32 v25, v24, 16, 1
	v_add3_u32 v24, v24, v25, s14
	ds_write_b16_d16_hi v238, v24 offset:816
	global_load_dword v24, v[194:195], off offset:576
	v_mul_f32_e32 v25, v78, v7
	s_waitcnt vmcnt(0)
	v_mul_f32_e32 v25, v25, v24
	v_bfe_u32 v26, v25, 16, 1
	v_add3_u32 v25, v25, v26, s14
	ds_write_b16_d16_hi v238, v25 offset:32
	v_mul_f32_e32 v25, v79, v84
	v_mul_f32_e32 v25, v25, v24
	v_bfe_u32 v26, v25, 16, 1
	v_add3_u32 v25, v25, v26, s14
	ds_write_b16_d16_hi v238, v25 offset:304
	v_mul_f32_e32 v25, v76, v85
	v_mul_f32_e32 v25, v25, v24
	v_bfe_u32 v26, v25, 16, 1
	v_add3_u32 v25, v25, v26, s14
	ds_write_b16_d16_hi v238, v25 offset:576
	v_mul_f32_e32 v25, v77, v88
	v_mul_f32_e32 v24, v25, v24
	v_bfe_u32 v25, v24, 16, 1
	v_add3_u32 v24, v24, v25, s14
	ds_write_b16_d16_hi v238, v24 offset:848
	global_load_dword v24, v[194:195], off offset:640
	v_mul_f32_e32 v25, v75, v7
	s_waitcnt vmcnt(0)
	v_mul_f32_e32 v25, v25, v24
	v_bfe_u32 v26, v25, 16, 1
	v_add3_u32 v25, v25, v26, s14
	ds_write_b16_d16_hi v238, v25 offset:64
	v_mul_f32_e32 v25, v71, v84
	v_mul_f32_e32 v25, v25, v24
	v_bfe_u32 v26, v25, 16, 1
	v_add3_u32 v25, v25, v26, s14
	ds_write_b16_d16_hi v238, v25 offset:336
	v_mul_f32_e32 v25, v73, v85
	v_mul_f32_e32 v25, v25, v24
	v_bfe_u32 v26, v25, 16, 1
	v_add3_u32 v25, v25, v26, s14
	ds_write_b16_d16_hi v238, v25 offset:608
	v_mul_f32_e32 v25, v69, v88
	v_mul_f32_e32 v24, v25, v24
	v_bfe_u32 v25, v24, 16, 1
	v_add3_u32 v24, v24, v25, s14
	ds_write_b16_d16_hi v238, v24 offset:880
	global_load_dword v24, v[194:195], off offset:704
	v_mul_f32_e32 v25, v74, v7
	s_waitcnt vmcnt(0)
	v_mul_f32_e32 v25, v25, v24
	v_bfe_u32 v26, v25, 16, 1
	v_add3_u32 v25, v25, v26, s14
	ds_write_b16_d16_hi v238, v25 offset:96
	v_mul_f32_e32 v25, v70, v84
	v_mul_f32_e32 v25, v25, v24
	v_bfe_u32 v26, v25, 16, 1
	v_add3_u32 v25, v25, v26, s14
	ds_write_b16_d16_hi v238, v25 offset:368
	v_mul_f32_e32 v25, v72, v85
	v_mul_f32_e32 v25, v25, v24
	v_bfe_u32 v26, v25, 16, 1
	v_add3_u32 v25, v25, v26, s14
	ds_write_b16_d16_hi v238, v25 offset:640
	v_mul_f32_e32 v25, v68, v88
	v_mul_f32_e32 v24, v25, v24
	v_bfe_u32 v25, v24, 16, 1
	v_add3_u32 v24, v24, v25, s14
	ds_write_b16_d16_hi v238, v24 offset:912
	global_load_dword v24, v[194:195], off offset:768
	v_mul_f32_e32 v25, v63, v7
	s_waitcnt vmcnt(0)
	v_mul_f32_e32 v25, v25, v24
	v_bfe_u32 v26, v25, 16, 1
	v_add3_u32 v25, v25, v26, s14
	ds_write_b16_d16_hi v238, v25 offset:128
	v_mul_f32_e32 v25, v65, v84
	v_mul_f32_e32 v25, v25, v24
	v_bfe_u32 v26, v25, 16, 1
	v_add3_u32 v25, v25, v26, s14
	ds_write_b16_d16_hi v238, v25 offset:400
	v_mul_f32_e32 v25, v67, v85
	v_mul_f32_e32 v25, v25, v24
	v_bfe_u32 v26, v25, 16, 1
	v_add3_u32 v25, v25, v26, s14
	ds_write_b16_d16_hi v238, v25 offset:672
	v_mul_f32_e32 v25, v61, v88
	v_mul_f32_e32 v24, v25, v24
	v_bfe_u32 v25, v24, 16, 1
	v_add3_u32 v24, v24, v25, s14
	ds_write_b16_d16_hi v238, v24 offset:944
	global_load_dword v24, v[194:195], off offset:832
	v_mul_f32_e32 v25, v62, v7
	s_waitcnt vmcnt(0)
	v_mul_f32_e32 v25, v25, v24
	v_bfe_u32 v26, v25, 16, 1
	v_add3_u32 v25, v25, v26, s14
	ds_write_b16_d16_hi v238, v25 offset:160
	v_mul_f32_e32 v25, v64, v84
	v_mul_f32_e32 v25, v25, v24
	v_bfe_u32 v26, v25, 16, 1
	v_add3_u32 v25, v25, v26, s14
	ds_write_b16_d16_hi v238, v25 offset:432
	v_mul_f32_e32 v25, v66, v85
	v_mul_f32_e32 v25, v25, v24
	v_bfe_u32 v26, v25, 16, 1
	v_add3_u32 v25, v25, v26, s14
	ds_write_b16_d16_hi v238, v25 offset:704
	v_mul_f32_e32 v25, v60, v88
	v_mul_f32_e32 v24, v25, v24
	v_bfe_u32 v25, v24, 16, 1
	v_add3_u32 v24, v24, v25, s14
	ds_write_b16_d16_hi v238, v24 offset:976
	global_load_dword v24, v[194:195], off offset:896
	v_mul_f32_e32 v25, v57, v7
	v_mul_f32_e32 v7, v56, v7
	s_waitcnt vmcnt(0)
	v_mul_f32_e32 v25, v25, v24
	v_bfe_u32 v26, v25, 16, 1
	v_add3_u32 v25, v25, v26, s14
	ds_write_b16_d16_hi v238, v25 offset:192
	v_mul_f32_e32 v25, v59, v84
	v_mul_f32_e32 v25, v25, v24
	v_bfe_u32 v26, v25, 16, 1
	v_add3_u32 v25, v25, v26, s14
	ds_write_b16_d16_hi v238, v25 offset:464
	v_mul_f32_e32 v25, v55, v85
	v_mul_f32_e32 v25, v25, v24
	v_bfe_u32 v26, v25, 16, 1
	v_add3_u32 v25, v25, v26, s14
	ds_write_b16_d16_hi v238, v25 offset:736
	v_mul_f32_e32 v25, v53, v88
	v_mul_f32_e32 v24, v25, v24
	v_bfe_u32 v25, v24, 16, 1
	v_add3_u32 v24, v24, v25, s14
	ds_write_b16_d16_hi v238, v24 offset:1008
	global_load_dword v24, v[194:195], off offset:960
	s_waitcnt vmcnt(0)
	v_mul_f32_e32 v7, v7, v24
	v_bfe_u32 v25, v7, 16, 1
	v_add3_u32 v7, v7, v25, s14
	ds_write_b16_d16_hi v238, v7 offset:224
	v_mul_f32_e32 v7, v58, v84
	v_mul_f32_e32 v7, v7, v24
	v_bfe_u32 v25, v7, 16, 1
	v_add3_u32 v7, v7, v25, s14
	ds_write_b16_d16_hi v238, v7 offset:496
	v_mul_f32_e32 v7, v54, v85
	v_mul_f32_e32 v7, v7, v24
	v_bfe_u32 v25, v7, 16, 1
	v_add3_u32 v7, v7, v25, s14
	ds_write_b16_d16_hi v238, v7 offset:768
	v_mul_f32_e32 v7, v52, v88
	v_mul_f32_e32 v7, v7, v24
	v_bfe_u32 v24, v7, 16, 1
	v_add3_u32 v7, v7, v24, s14
	ds_write_b16_d16_hi v238, v7 offset:1040
	s_and_saveexec_b64 s[80:81], s[76:77]
	s_cbranch_execz .LBB0_754
	v_lshlrev_b32_e32 v7, 16, v20
	v_mul_f32_e32 v7, 0xbfb8aa3b, v7
	v_exp_f32_e32 v28, v7
	v_and_b32_e32 v7, 0xffff0000, v20
	v_mul_f32_e32 v7, 0xbfb8aa3b, v7
	v_exp_f32_e32 v20, v7
	v_lshlrev_b32_e32 v7, 16, v21
	ds_read_b128 v[24:27], v239
	v_mul_f32_e32 v7, 0xbfb8aa3b, v7
	v_exp_f32_e32 v29, v7
	v_and_b32_e32 v7, 0xffff0000, v21
	v_mul_f32_e32 v7, 0xbfb8aa3b, v7
	s_waitcnt lgkmcnt(0)
	v_lshlrev_b32_e32 v30, 16, v25
	v_pk_add_f32 v[28:29], v[28:29], 1.0 op_sel_hi:[1,0]
	v_exp_f32_e32 v21, v7
	v_rcp_f32_e32 v32, v29
	v_lshlrev_b32_e32 v7, 16, v24
	v_and_b32_e32 v24, 0xffff0000, v24
	v_pk_add_f32 v[20:21], v[20:21], 1.0 op_sel_hi:[1,0]
	v_mul_f32_e32 v29, v30, v32
	v_rcp_f32_e32 v31, v28
	v_and_b32_e32 v25, 0xffff0000, v25
	v_mul_f32_e32 v7, v7, v31
	v_rcp_f32_e32 v30, v20
	s_nop 0
	v_mul_f32_e32 v24, v24, v30
	v_rcp_f32_e32 v28, v21
	s_nop 0
	v_mul_f32_e32 v25, v25, v28
	v_and_b32_e32 v21, 0xffff0000, v22
	v_mul_f32_e32 v21, 0xbfb8aa3b, v21
	v_lshlrev_b32_e32 v20, 16, v22
	v_exp_f32_e32 v22, v21
	v_lshlrev_b32_e32 v21, 16, v23
	v_mul_f32_e32 v20, 0xbfb8aa3b, v20
	v_mul_f32_e32 v21, 0xbfb8aa3b, v21
	v_exp_f32_e32 v20, v20
	v_exp_f32_e32 v21, v21
	v_lshlrev_b32_e32 v30, 16, v27
	v_lshlrev_b32_e32 v28, 16, v26
	v_and_b32_e32 v23, 0xffff0000, v23
	v_pk_add_f32 v[20:21], v[20:21], 1.0 op_sel_hi:[1,0]
	v_mul_f32_e32 v23, 0xbfb8aa3b, v23
	v_rcp_f32_e32 v32, v21
	v_exp_f32_e32 v23, v23
	v_and_b32_e32 v26, 0xffff0000, v26
	v_and_b32_e32 v27, 0xffff0000, v27
	v_mul_f32_e32 v30, v30, v32
	v_rcp_f32_e32 v31, v20
	s_nop 0
	v_mul_f32_e32 v28, v28, v31
	v_pk_add_f32 v[20:21], v[22:23], 1.0 op_sel_hi:[1,0]
	s_nop 0
	v_rcp_f32_e32 v23, v20
	s_nop 0
	v_mul_f32_e32 v20, v26, v23
	v_rcp_f32_e32 v23, v21
	s_nop 0
	v_mul_f32_e32 v21, v27, v23
	v_bfe_u32 v22, v21, 16, 1
	v_bfe_u32 v23, v20, 16, 1
	v_bfe_u32 v26, v25, 16, 1
	v_bfe_u32 v27, v24, 16, 1
	v_add3_u32 v24, v24, v27, s14
	v_add3_u32 v25, v25, v26, s14
	v_add3_u32 v20, v20, v23, s14
	v_add3_u32 v21, v21, v22, s14
	v_bfe_u32 v22, v7, 16, 1
	v_bfe_u32 v23, v29, 16, 1
	v_bfe_u32 v26, v28, 16, 1
	v_bfe_u32 v27, v30, 16, 1
	v_add3_u32 v27, v30, v27, s14
	v_add3_u32 v26, v28, v26, s14
	v_add3_u32 v23, v29, v23, s14
	v_add3_u32 v7, v7, v22, s14
	v_lshrrev_b32_e32 v7, 16, v7
	v_lshrrev_b32_e32 v28, 16, v23
	v_lshrrev_b32_e32 v22, 16, v26
	v_lshrrev_b32_e32 v23, 16, v27
	v_and_or_b32 v23, v21, s17, v23
	v_and_or_b32 v22, v20, s17, v22
	v_and_or_b32 v21, v25, s17, v28
	v_and_or_b32 v20, v24, s17, v7
	v_lshlrev_b64 v[24:25], 11, v[50:51]
	v_lshl_add_u64 v[24:25], v[176:177], 0, v[24:25]
	global_store_dwordx4 v[24:25], v[20:23], off offset:256 sc1
	s_or_b64 exec, exec, s[80:81]
	s_and_saveexec_b64 s[76:77], s[74:75]
	s_cbranch_execnz .LBB0_755

.LBB0_753:
	v_lshlrev_b32_e32 v7, 16, v12
	v_mul_f32_e32 v7, 0xbfb8aa3b, v7
	v_exp_f32_e32 v20, v7
	v_and_b32_e32 v7, 0xffff0000, v12
	v_mul_f32_e32 v7, 0xbfb8aa3b, v7
	v_exp_f32_e32 v12, v7
	v_lshlrev_b32_e32 v7, 16, v13
	ds_read_b128 v[16:19], v239 offset:2176
	v_mul_f32_e32 v7, 0xbfb8aa3b, v7
	v_exp_f32_e32 v21, v7
	v_and_b32_e32 v7, 0xffff0000, v13
	v_mul_f32_e32 v7, 0xbfb8aa3b, v7
	s_waitcnt lgkmcnt(0)
	v_lshlrev_b32_e32 v22, 16, v17
	v_pk_add_f32 v[20:21], v[20:21], 1.0 op_sel_hi:[1,0]
	v_exp_f32_e32 v13, v7
	v_rcp_f32_e32 v24, v21
	v_lshlrev_b32_e32 v7, 16, v16
	v_and_b32_e32 v16, 0xffff0000, v16
	v_pk_add_f32 v[12:13], v[12:13], 1.0 op_sel_hi:[1,0]
	v_mul_f32_e32 v21, v22, v24
	v_rcp_f32_e32 v23, v20
	v_and_b32_e32 v17, 0xffff0000, v17
	v_mul_f32_e32 v7, v7, v23
	v_rcp_f32_e32 v22, v12
	s_nop 0
	v_mul_f32_e32 v16, v16, v22
	v_rcp_f32_e32 v20, v13
	s_nop 0
	v_mul_f32_e32 v17, v17, v20
	v_and_b32_e32 v13, 0xffff0000, v14
	v_mul_f32_e32 v13, 0xbfb8aa3b, v13
	v_lshlrev_b32_e32 v12, 16, v14
	v_exp_f32_e32 v14, v13
	v_lshlrev_b32_e32 v13, 16, v15
	v_mul_f32_e32 v12, 0xbfb8aa3b, v12
	v_mul_f32_e32 v13, 0xbfb8aa3b, v13
	v_exp_f32_e32 v12, v12
	v_exp_f32_e32 v13, v13
	v_lshlrev_b32_e32 v22, 16, v19
	v_lshlrev_b32_e32 v20, 16, v18
	v_and_b32_e32 v15, 0xffff0000, v15
	v_pk_add_f32 v[12:13], v[12:13], 1.0 op_sel_hi:[1,0]
	v_mul_f32_e32 v15, 0xbfb8aa3b, v15
	v_rcp_f32_e32 v24, v13
	v_exp_f32_e32 v15, v15
	v_and_b32_e32 v18, 0xffff0000, v18
	v_and_b32_e32 v19, 0xffff0000, v19
	v_mul_f32_e32 v22, v22, v24
	v_rcp_f32_e32 v23, v12
	s_nop 0
	v_mul_f32_e32 v20, v20, v23
	v_pk_add_f32 v[12:13], v[14:15], 1.0 op_sel_hi:[1,0]
	s_nop 0
	v_rcp_f32_e32 v15, v12
	s_nop 0
	v_mul_f32_e32 v12, v18, v15
	v_rcp_f32_e32 v15, v13
	s_nop 0
	v_mul_f32_e32 v13, v19, v15
	v_bfe_u32 v14, v13, 16, 1
	v_bfe_u32 v15, v12, 16, 1
	v_bfe_u32 v18, v17, 16, 1
	v_bfe_u32 v19, v16, 16, 1
	v_add3_u32 v16, v16, v19, s14
	v_add3_u32 v17, v17, v18, s14
	v_add3_u32 v12, v12, v15, s14
	v_add3_u32 v13, v13, v14, s14
	v_bfe_u32 v14, v7, 16, 1
	v_bfe_u32 v15, v21, 16, 1
	v_bfe_u32 v18, v20, 16, 1
	v_bfe_u32 v19, v22, 16, 1
	v_add3_u32 v19, v22, v19, s14
	v_add3_u32 v18, v20, v18, s14
	v_add3_u32 v15, v21, v15, s14
	v_add3_u32 v7, v7, v14, s14
	v_lshrrev_b32_e32 v7, 16, v7
	v_lshrrev_b32_e32 v20, 16, v15
	v_lshrrev_b32_e32 v14, 16, v18
	v_lshrrev_b32_e32 v15, 16, v19
	v_and_or_b32 v15, v13, s17, v15
	v_and_or_b32 v14, v12, s17, v14
	v_and_or_b32 v13, v17, s17, v20
	v_and_or_b32 v12, v16, s17, v7
	v_lshlrev_b64 v[16:17], 11, v[46:47]
	v_lshl_add_u64 v[16:17], v[176:177], 0, v[16:17]
	global_store_dwordx4 v[16:17], v[12:15], off offset:256 sc1
	s_or_b64 exec, exec, s[74:75]
	s_and_saveexec_b64 s[72:73], s[70:71]
	s_cbranch_execz .LBB0_688
	s_branch .LBB0_757

.LBB0_755:
	v_lshlrev_b32_e32 v7, 16, v16
	v_mul_f32_e32 v7, 0xbfb8aa3b, v7
	v_exp_f32_e32 v24, v7
	v_and_b32_e32 v7, 0xffff0000, v16
	v_mul_f32_e32 v7, 0xbfb8aa3b, v7
	v_exp_f32_e32 v16, v7
	v_lshlrev_b32_e32 v7, 16, v17
	ds_read_b128 v[20:23], v239 offset:1088
	v_mul_f32_e32 v7, 0xbfb8aa3b, v7
	v_exp_f32_e32 v25, v7
	v_and_b32_e32 v7, 0xffff0000, v17
	v_mul_f32_e32 v7, 0xbfb8aa3b, v7
	s_waitcnt lgkmcnt(0)
	v_lshlrev_b32_e32 v26, 16, v21
	v_pk_add_f32 v[24:25], v[24:25], 1.0 op_sel_hi:[1,0]
	v_exp_f32_e32 v17, v7
	v_rcp_f32_e32 v28, v25
	v_lshlrev_b32_e32 v7, 16, v20
	v_and_b32_e32 v20, 0xffff0000, v20
	v_pk_add_f32 v[16:17], v[16:17], 1.0 op_sel_hi:[1,0]
	v_mul_f32_e32 v25, v26, v28
	v_rcp_f32_e32 v27, v24
	v_and_b32_e32 v21, 0xffff0000, v21
	v_mul_f32_e32 v7, v7, v27
	v_rcp_f32_e32 v26, v16
	s_nop 0
	v_mul_f32_e32 v20, v20, v26
	v_rcp_f32_e32 v24, v17
	s_nop 0
	v_mul_f32_e32 v21, v21, v24
	v_and_b32_e32 v17, 0xffff0000, v18
	v_mul_f32_e32 v17, 0xbfb8aa3b, v17
	v_lshlrev_b32_e32 v16, 16, v18
	v_exp_f32_e32 v18, v17
	v_lshlrev_b32_e32 v17, 16, v19
	v_mul_f32_e32 v16, 0xbfb8aa3b, v16
	v_mul_f32_e32 v17, 0xbfb8aa3b, v17
	v_exp_f32_e32 v16, v16
	v_exp_f32_e32 v17, v17
	v_lshlrev_b32_e32 v26, 16, v23
	v_lshlrev_b32_e32 v24, 16, v22
	v_and_b32_e32 v19, 0xffff0000, v19
	v_pk_add_f32 v[16:17], v[16:17], 1.0 op_sel_hi:[1,0]
	v_mul_f32_e32 v19, 0xbfb8aa3b, v19
	v_rcp_f32_e32 v28, v17
	v_exp_f32_e32 v19, v19
	v_and_b32_e32 v22, 0xffff0000, v22
	v_and_b32_e32 v23, 0xffff0000, v23
	v_mul_f32_e32 v26, v26, v28
	v_rcp_f32_e32 v27, v16
	s_nop 0
	v_mul_f32_e32 v24, v24, v27
	v_pk_add_f32 v[16:17], v[18:19], 1.0 op_sel_hi:[1,0]
	s_nop 0
	v_rcp_f32_e32 v19, v16
	s_nop 0
	v_mul_f32_e32 v16, v22, v19
	v_rcp_f32_e32 v19, v17
	s_nop 0
	v_mul_f32_e32 v17, v23, v19
	v_bfe_u32 v18, v17, 16, 1
	v_bfe_u32 v19, v16, 16, 1
	v_bfe_u32 v22, v21, 16, 1
	v_bfe_u32 v23, v20, 16, 1
	v_add3_u32 v20, v20, v23, s14
	v_add3_u32 v21, v21, v22, s14
	v_add3_u32 v16, v16, v19, s14
	v_add3_u32 v17, v17, v18, s14
	v_bfe_u32 v18, v7, 16, 1
	v_bfe_u32 v19, v25, 16, 1
	v_bfe_u32 v22, v24, 16, 1
	v_bfe_u32 v23, v26, 16, 1
	v_add3_u32 v23, v26, v23, s14
	v_add3_u32 v22, v24, v22, s14
	v_add3_u32 v19, v25, v19, s14
	v_add3_u32 v7, v7, v18, s14
	v_lshrrev_b32_e32 v7, 16, v7
	v_lshrrev_b32_e32 v24, 16, v19
	v_lshrrev_b32_e32 v18, 16, v22
	v_lshrrev_b32_e32 v19, 16, v23
	v_and_or_b32 v19, v17, s17, v19
	v_and_or_b32 v18, v16, s17, v18
	v_and_or_b32 v17, v21, s17, v24
	v_and_or_b32 v16, v20, s17, v7
	v_lshlrev_b64 v[20:21], 11, v[48:49]
	v_lshl_add_u64 v[20:21], v[176:177], 0, v[20:21]
	global_store_dwordx4 v[20:21], v[16:19], off offset:256 sc1
	s_or_b64 exec, exec, s[76:77]
	s_and_saveexec_b64 s[74:75], s[72:73]
	s_cbranch_execnz .LBB0_753

.LBB0_757:
	v_lshlrev_b32_e32 v7, 16, v8
	v_mul_f32_e32 v7, 0xbfb8aa3b, v7
	v_exp_f32_e32 v16, v7
	v_and_b32_e32 v7, 0xffff0000, v8
	v_mul_f32_e32 v7, 0xbfb8aa3b, v7
	v_exp_f32_e32 v8, v7
	v_lshlrev_b32_e32 v7, 16, v9
	ds_read_b128 v[12:15], v239 offset:3264
	v_mul_f32_e32 v7, 0xbfb8aa3b, v7
	v_exp_f32_e32 v17, v7
	v_and_b32_e32 v7, 0xffff0000, v9
	v_mul_f32_e32 v7, 0xbfb8aa3b, v7
	s_waitcnt lgkmcnt(0)
	v_lshlrev_b32_e32 v18, 16, v13
	v_pk_add_f32 v[16:17], v[16:17], 1.0 op_sel_hi:[1,0]
	v_exp_f32_e32 v9, v7
	v_rcp_f32_e32 v20, v17
	v_lshlrev_b32_e32 v7, 16, v12
	v_and_b32_e32 v12, 0xffff0000, v12
	v_pk_add_f32 v[8:9], v[8:9], 1.0 op_sel_hi:[1,0]
	v_mul_f32_e32 v17, v18, v20
	v_rcp_f32_e32 v19, v16
	v_and_b32_e32 v13, 0xffff0000, v13
	v_mul_f32_e32 v7, v7, v19
	v_rcp_f32_e32 v18, v8
	s_nop 0
	v_mul_f32_e32 v12, v12, v18
	v_rcp_f32_e32 v16, v9
	s_nop 0
	v_mul_f32_e32 v13, v13, v16
	v_and_b32_e32 v9, 0xffff0000, v10
	v_mul_f32_e32 v9, 0xbfb8aa3b, v9
	v_lshlrev_b32_e32 v8, 16, v10
	v_exp_f32_e32 v10, v9
	v_lshlrev_b32_e32 v9, 16, v11
	v_mul_f32_e32 v8, 0xbfb8aa3b, v8
	v_mul_f32_e32 v9, 0xbfb8aa3b, v9
	v_exp_f32_e32 v8, v8
	v_exp_f32_e32 v9, v9
	v_lshlrev_b32_e32 v18, 16, v15
	v_lshlrev_b32_e32 v16, 16, v14
	v_and_b32_e32 v11, 0xffff0000, v11
	v_pk_add_f32 v[8:9], v[8:9], 1.0 op_sel_hi:[1,0]
	v_mul_f32_e32 v11, 0xbfb8aa3b, v11
	v_rcp_f32_e32 v20, v9
	v_exp_f32_e32 v11, v11
	v_and_b32_e32 v14, 0xffff0000, v14
	v_and_b32_e32 v15, 0xffff0000, v15
	v_mul_f32_e32 v18, v18, v20
	v_rcp_f32_e32 v19, v8
	s_nop 0
	v_mul_f32_e32 v16, v16, v19
	v_pk_add_f32 v[8:9], v[10:11], 1.0 op_sel_hi:[1,0]
	s_nop 0
	v_rcp_f32_e32 v11, v8
	s_nop 0
	v_mul_f32_e32 v8, v14, v11
	v_rcp_f32_e32 v11, v9
	s_nop 0
	v_mul_f32_e32 v9, v15, v11
	v_bfe_u32 v10, v9, 16, 1
	v_bfe_u32 v11, v8, 16, 1
	v_bfe_u32 v14, v13, 16, 1
	v_bfe_u32 v15, v12, 16, 1
	v_add3_u32 v12, v12, v15, s14
	v_add3_u32 v13, v13, v14, s14
	v_add3_u32 v8, v8, v11, s14
	v_add3_u32 v9, v9, v10, s14
	v_bfe_u32 v10, v7, 16, 1
	v_bfe_u32 v11, v17, 16, 1
	v_bfe_u32 v14, v16, 16, 1
	v_bfe_u32 v15, v18, 16, 1
	v_add3_u32 v15, v18, v15, s14
	v_add3_u32 v14, v16, v14, s14
	v_add3_u32 v11, v17, v11, s14
	v_add3_u32 v7, v7, v10, s14
	v_lshrrev_b32_e32 v7, 16, v7
	v_lshrrev_b32_e32 v16, 16, v11
	v_lshrrev_b32_e32 v10, 16, v14
	v_lshrrev_b32_e32 v11, 16, v15
	v_and_or_b32 v11, v9, s17, v11
	v_and_or_b32 v10, v8, s17, v10
	v_and_or_b32 v9, v13, s17, v16
	v_and_or_b32 v8, v12, s17, v7
	v_lshlrev_b64 v[12:13], 11, v[44:45]
	v_lshl_add_u64 v[12:13], v[176:177], 0, v[12:13]
	global_store_dwordx4 v[12:13], v[8:11], off offset:256 sc1
	s_branch .LBB0_688
